# E6 + GEMM pipeline prologue: tile-1 stage loads issued before the wr==1 stagger barrier and first wait (vmcnt 2->8), 24 sites
# baseline (speedup 1.0000x reference)
.LBB0_253:
	s_add_u32 s8, s14, 0x2a000000
	s_addc_u32 s9, s15, 0
	s_add_u32 s12, s14, 0x2e000000
	s_addc_u32 s13, s15, 0
	s_add_u32 s14, s14, 0x4b200000
	s_addc_u32 s15, s15, 0
	s_lshl_b32 s16, s16, 5
	s_and_b32 s22, s16, 0x60
	s_mov_b64 s[16:17], 0x80
	s_add_i32 m0, s53, 0x18000
	v_lshl_add_u64 v[6:7], v[6:7], 0, s[16:17]
	s_lshl_b32 s19, s18, 13
	s_lshl_b32 s23, s22, 7
	global_load_lds_dwordx4 v[6:7], off
	v_lshl_add_u64 v[4:5], v[4:5], 0, s[16:17]
	s_add_i32 m0, s53, 0x1a000
	s_add_i32 s57, s53, 0x8000
	s_add_i32 s58, s53, 0xa000
	global_load_lds_dwordx4 v[4:5], off
	v_lshl_add_u64 v[0:1], v[0:1], 0, s[16:17]
	s_mov_b32 m0, s57
	s_add_u32 s20, s36, 0x40080
	global_load_lds_dwordx4 v[0:1], off
	v_lshl_add_u64 v[0:1], v[2:3], 0, s[16:17]
	s_mov_b32 m0, s58
	s_addc_u32 s21, s37, 0
	global_load_lds_dwordx4 v[0:1], off
	s_add_i32 m0, s53, 0x1c000
	v_lshl_add_u64 v[0:1], s[20:21], 0, v[132:133]
	global_load_lds_dwordx4 v[0:1], off
	v_lshl_add_u64 v[0:1], s[20:21], 0, v[128:129]
	s_add_i32 m0, s53, 0x1e000
	s_mov_b64 s[20:21], 0x40080
	global_load_lds_dwordx4 v[0:1], off
	s_cmp_lg_u32 s18, 1
	s_cbranch_scc1 .Lpgh_0
	s_barrier
.Lpgh_0:
	s_waitcnt vmcnt(8)
	s_barrier
	v_lshrrev_b32_e32 v1, 1, v9
	v_and_b32_e32 v1, 24, v1
	v_and_b32_e32 v0, 15, v9
	v_lshlrev_b32_e32 v2, 1, v1
	v_lshl_or_b32 v147, s18, 6, v0
	v_lshl_or_b32 v0, v0, 6, v2
	v_lshlrev_b32_e32 v2, 2, v9
	v_and_b32_e32 v2, 32, v2
	v_bitop3_b32 v3, v0, s19, v2 bitop3:0xde
	v_bitop3_b32 v149, s23, v0, v2 bitop3:0xf6
	v_lshlrev_b32_e32 v0, 4, v12
	v_or_b32_e32 v153, s22, v1
	v_and_b32_e32 v0, 0xffff8000, v0
	v_lshlrev_b32_e32 v1, 11, v13
	v_or3_b32 v0, v10, v0, v1
	v_add_u32_e32 v136, v0, v11
	v_lshlrev_b32_e32 v0, 4, v8
	v_and_b32_e32 v0, 0xffff8000, v0
	s_waitcnt vmcnt(6)
	s_cmpk_lt_u32 s3, 0x100
	v_or3_b32 v0, v10, v0, v1
	s_cselect_b64 s[18:19], -1, 0
	v_lshl_add_u64 v[138:139], v[136:137], 0, s[20:21]
	v_add_u32_e32 v136, v0, v11
	s_add_i32 s61, 0, 0x10000
	s_add_i32 s62, 0, 0x14000
	s_sext_i32_i8 s63, s2
	s_mov_b32 s59, 0
	v_or_b32_e32 v157, 0xfffffe00, v153
	s_ashr_i32 s60, s44, 31
	v_lshl_add_u64 v[140:141], v[136:137], 0, s[20:21]
	v_mov_b64_e32 v[142:143], 0x600
	v_mov_b64_e32 v[144:145], 0x5ff
	v_add_u32_e32 v161, s61, v149
	v_add_u32_e32 v165, s62, v149
	v_add_u32_e32 v169, 0, v3
	s_mov_b64 s[26:27], s[36:37]
	s_mov_b64 s[24:25], s[30:31]
	s_barrier
	s_branch .LBB0_256

.LBB0_420:
	s_add_u32 s14, s16, 0x26000000
	s_addc_u32 s15, s17, 0
	s_add_u32 s16, s16, 0x4b000000
	s_mov_b64 s[18:19], 0x80
	s_addc_u32 s17, s17, 0
	s_and_b32 s55, s3, 3
	s_add_i32 m0, s51, 0x18000
	v_lshl_add_u64 v[6:7], v[6:7], 0, s[18:19]
	s_lshl_b32 s3, s2, 13
	s_lshl_b32 s21, s55, 12
	global_load_lds_dwordx4 v[6:7], off
	v_lshl_add_u64 v[4:5], v[4:5], 0, s[18:19]
	s_add_i32 m0, s51, 0x1a000
	s_add_i32 s56, s51, 0x8000
	s_add_i32 s57, s51, 0xa000
	global_load_lds_dwordx4 v[4:5], off
	v_lshl_add_u64 v[0:1], v[0:1], 0, s[18:19]
	s_mov_b32 m0, s56
	s_add_u32 s4, s36, 0x40080
	global_load_lds_dwordx4 v[0:1], off
	v_lshl_add_u64 v[0:1], v[2:3], 0, s[18:19]
	s_mov_b32 m0, s57
	s_addc_u32 s5, s37, 0
	global_load_lds_dwordx4 v[0:1], off
	s_add_i32 m0, s51, 0x1c000
	v_lshl_add_u64 v[0:1], s[4:5], 0, v[194:195]
	global_load_lds_dwordx4 v[0:1], off
	v_lshl_add_u64 v[0:1], s[4:5], 0, v[198:199]
	s_add_i32 m0, s51, 0x1e000
	s_movk_i32 s22, 0x80
	global_load_lds_dwordx4 v[0:1], off
	s_cmp_lg_u32 s2, 1
	s_cbranch_scc1 .Lpgh_1
	s_barrier
.Lpgh_1:
	s_waitcnt vmcnt(8)
	s_barrier
	v_bfe_u32 v1, v9, 4, 2
	v_and_b32_e32 v0, 15, v9
	v_lshlrev_b32_e32 v3, 4, v1
	v_lshl_or_b32 v240, s2, 6, v0
	v_lshl_or_b32 v0, v0, 6, v3
	v_lshlrev_b32_e32 v3, 2, v9
	v_and_b32_e32 v3, 32, v3
	v_lshlrev_b32_e32 v2, 3, v1
	v_bitop3_b32 v4, v0, s3, v3 bitop3:0xde
	v_bitop3_b32 v241, v0, s21, v3 bitop3:0xde
	v_cmp_eq_u32_e64 s[2:3], 0, v1
	v_lshlrev_b32_e32 v0, 2, v8
	v_bfrev_b32_e32 v1, 0.5
	v_bitop3_b32 v243, v0, 64, v1 bitop3:0x6c
	v_bitop3_b32 v244, v0, s22, v1 bitop3:0x6c
	v_lshlrev_b32_e32 v0, 4, v14
	v_lshl_or_b32 v242, s55, 5, v2
	v_and_b32_e32 v0, 0xffff8000, v0
	v_lshlrev_b32_e32 v2, 11, v13
	v_or3_b32 v0, v11, v0, v2
	s_mov_b64 s[4:5], 0x40080
	v_add_u32_e32 v0, v0, v12
	v_mov_b32_e32 v1, v195
	v_lshl_add_u64 v[200:201], v[0:1], 0, s[4:5]
	v_lshlrev_b32_e32 v0, 4, v10
	v_and_b32_e32 v0, 0xffff8000, v0
	s_waitcnt vmcnt(6)
	s_cmpk_lt_u32 s20, 0x100
	v_or3_b32 v0, v11, v0, v2
	s_cselect_b64 s[20:21], -1, 0
	v_add_u32_e32 v0, v0, v12
	s_add_i32 s60, 0, 0x10000
	s_add_i32 s61, 0, 0x14000
	s_ashr_i32 s58, s44, 31
	s_ashr_i32 s59, s49, 31
	v_lshl_add_u64 v[202:203], v[0:1], 0, s[4:5]
	v_mov_b64_e32 v[204:205], 0x200
	v_mov_b64_e32 v[206:207], 0x1ff
	v_add_u32_e32 v245, s60, v241
	v_add_u32_e32 v246, s61, v241
	v_add_u32_e32 v247, 0, v4
	s_mov_b32 s62, 0
	s_mov_b64 s[26:27], s[30:31]
	s_mov_b64 s[28:29], s[36:37]
	s_barrier
	s_branch .LBB0_423

.LBB0_535:
	v_bfe_u32 v82, v8, 4, 2
	v_and_b32_e32 v10, 15, v8
	v_lshlrev_b32_e32 v11, 4, v82
	v_lshlrev_b32_e32 v8, 2, v8
	s_and_b32 s55, s2, 3
	v_lshl_or_b32 v81, s3, 6, v10
	v_lshl_or_b32 v10, v10, 6, v11
	s_lshl_b32 s2, s3, 13
	v_and_b32_e32 v8, 32, v8
	v_bitop3_b32 v12, v10, s2, v8 bitop3:0xde
	s_lshl_b32 s2, s55, 12
	v_bitop3_b32 v83, v10, s2, v8 bitop3:0xde
	s_add_u32 s2, s30, 0x1e00080
	s_addc_u32 s3, s31, 0
	s_add_i32 m0, s9, 0x18000
	v_lshl_add_u64 v[10:11], s[2:3], 0, v[64:65]
	global_load_lds_dwordx4 v[10:11], off
	v_lshl_add_u64 v[10:11], s[2:3], 0, v[66:67]
	s_add_i32 m0, s9, 0x1a000
	s_mov_b64 s[16:17], 0x80
	s_add_i32 s59, s9, 0x8000
	s_add_i32 s60, s9, 0xa000
	global_load_lds_dwordx4 v[10:11], off
	v_lshl_add_u64 v[0:1], v[0:1], 0, s[16:17]
	s_mov_b32 m0, s59
	s_add_u32 s2, s30, 0x1e40080
	global_load_lds_dwordx4 v[0:1], off
	v_lshl_add_u64 v[0:1], v[2:3], 0, s[16:17]
	s_mov_b32 m0, s60
	s_addc_u32 s3, s31, 0
	s_add_i32 s61, s9, 0x1c000
	global_load_lds_dwordx4 v[0:1], off
	v_lshl_add_u64 v[0:1], s[2:3], 0, v[64:65]
	s_mov_b32 m0, s61
	s_add_i32 s62, s9, 0x1e000
	global_load_lds_dwordx4 v[0:1], off
	v_lshl_add_u64 v[0:1], s[2:3], 0, v[66:67]
	s_mov_b32 m0, s62
	v_lshlrev_b32_e32 v2, 11, v7
	global_load_lds_dwordx4 v[0:1], off
	s_cmp_eq_u64 s[14:15], 0
	s_cbranch_scc1 .Lpgh_2
	s_barrier
.Lpgh_2:
	s_waitcnt vmcnt(8)
	s_barrier
	v_lshlrev_b32_e32 v0, 4, v9
	v_and_b32_e32 v0, 0xffff8000, v0
	v_or3_b32 v0, v5, v0, v2
	v_add_u32_e32 v0, v0, v6
	v_mov_b32_e32 v1, v65
	s_mov_b64 s[2:3], 0x40080
	v_lshl_add_u64 v[68:69], v[0:1], 0, s[2:3]
	v_lshlrev_b32_e32 v0, 4, v4
	v_and_b32_e32 v0, 0xffff8000, v0
	s_waitcnt vmcnt(6)
	v_or3_b32 v0, v5, v0, v2
	s_cmpk_lt_u32 s4, 0x100
	v_add_u32_e32 v0, v0, v6
	s_cselect_b64 s[18:19], -1, 0
	v_lshl_add_u64 v[70:71], v[0:1], 0, s[2:3]
	v_mov_b64_e32 v[72:73], 0x80
	v_mov_b64_e32 v[74:75], 0x7f
	s_add_i32 s63, 0, 0x10000
	v_add_u32_e32 v84, 0, v12
	s_mov_b64 s[36:37], s[12:13]
	v_mov_b32_e32 v0, v65
	v_mov_b32_e32 v2, v65
	v_mov_b32_e32 v3, v65
	v_mov_b32_e32 v4, v65
	v_mov_b32_e32 v5, v65
	v_mov_b32_e32 v6, v65
	v_mov_b32_e32 v7, v65
	v_mov_b32_e32 v8, v65
	v_mov_b32_e32 v9, v65
	v_mov_b32_e32 v10, v65
	v_mov_b32_e32 v11, v65
	v_mov_b32_e32 v12, v65
	v_mov_b32_e32 v13, v65
	v_mov_b32_e32 v14, v65
	v_mov_b32_e32 v15, v65
	v_mov_b32_e32 v16, v65
	v_mov_b32_e32 v17, v65
	v_mov_b32_e32 v18, v65
	v_mov_b32_e32 v19, v65
	v_mov_b32_e32 v20, v65
	v_mov_b32_e32 v21, v65
	v_mov_b32_e32 v22, v65
	v_mov_b32_e32 v23, v65
	v_mov_b32_e32 v24, v65
	v_mov_b32_e32 v25, v65
	v_mov_b32_e32 v26, v65
	v_mov_b32_e32 v27, v65
	v_mov_b32_e32 v28, v65
	v_mov_b32_e32 v29, v65
	v_mov_b32_e32 v30, v65
	v_mov_b32_e32 v31, v65
	v_mov_b32_e32 v32, v65
	v_mov_b32_e32 v33, v65
	v_mov_b32_e32 v34, v65
	v_mov_b32_e32 v35, v65
	v_mov_b32_e32 v36, v65
	v_mov_b32_e32 v37, v65
	v_mov_b32_e32 v38, v65
	v_mov_b32_e32 v39, v65
	v_mov_b32_e32 v40, v65
	v_mov_b32_e32 v41, v65
	v_mov_b32_e32 v42, v65
	v_mov_b32_e32 v43, v65
	v_mov_b32_e32 v44, v65
	v_mov_b32_e32 v45, v65
	v_mov_b32_e32 v46, v65
	v_mov_b32_e32 v47, v65
	v_mov_b32_e32 v48, v65
	v_mov_b32_e32 v49, v65
	v_mov_b32_e32 v50, v65
	v_mov_b32_e32 v51, v65
	v_mov_b32_e32 v52, v65
	v_mov_b32_e32 v53, v65
	v_mov_b32_e32 v54, v65
	v_mov_b32_e32 v55, v65
	v_mov_b32_e32 v56, v65
	v_mov_b32_e32 v57, v65
	v_mov_b32_e32 v58, v65
	v_mov_b32_e32 v59, v65
	v_mov_b32_e32 v60, v65
	v_mov_b32_e32 v61, v65
	v_mov_b32_e32 v62, v65
	v_mov_b32_e32 v63, v65
	s_mov_b64 s[24:25], s[22:23]
	s_mov_b64 s[26:27], s[12:13]
	s_barrier
	s_branch .LBB0_538

.LBB0_775:
	s_add_u32 s14, s2, 0x34000000
	s_addc_u32 s15, s3, 0
	s_add_u32 s16, s2, 0x41000000
	s_addc_u32 s17, s3, 0
	s_lshl_b32 s2, s18, 5
	s_mov_b64 s[18:19], 0x80
	s_and_b32 s23, s2, 0x60
	s_add_i32 m0, s50, 0x18000
	v_lshl_add_u64 v[6:7], v[6:7], 0, s[18:19]
	s_lshl_b32 s22, s21, 13
	s_lshl_b32 s24, s23, 7
	global_load_lds_dwordx4 v[6:7], off
	v_lshl_add_u64 v[4:5], v[4:5], 0, s[18:19]
	s_add_i32 m0, s50, 0x1a000
	s_add_i32 s55, s50, 0x8000
	s_add_i32 s56, s50, 0xa000
	global_load_lds_dwordx4 v[4:5], off
	v_lshl_add_u64 v[0:1], v[0:1], 0, s[18:19]
	s_mov_b32 m0, s55
	s_add_u32 s2, s36, 0x40080
	global_load_lds_dwordx4 v[0:1], off
	v_lshl_add_u64 v[0:1], v[2:3], 0, s[18:19]
	s_mov_b32 m0, s56
	s_addc_u32 s3, s37, 0
	global_load_lds_dwordx4 v[0:1], off
	s_add_i32 m0, s50, 0x1c000
	v_lshl_add_u64 v[0:1], s[2:3], 0, v[128:129]
	global_load_lds_dwordx4 v[0:1], off
	v_lshl_add_u64 v[0:1], s[2:3], 0, v[130:131]
	s_add_i32 m0, s50, 0x1e000
	global_load_lds_dwordx4 v[0:1], off
	s_cmp_lg_u32 s21, 1
	s_cbranch_scc1 .Lpgh_3
	s_barrier
.Lpgh_3:
	s_waitcnt vmcnt(8)
	s_barrier
	s_cmpk_lt_u32 s20, 0x100
	v_lshrrev_b32_e32 v1, 1, v8
	v_and_b32_e32 v1, 24, v1
	v_and_b32_e32 v0, 15, v8
	v_lshlrev_b32_e32 v2, 1, v1
	v_lshl_or_b32 v137, s21, 6, v0
	v_lshl_or_b32 v0, v0, 6, v2
	v_lshlrev_b32_e32 v2, 2, v8
	v_and_b32_e32 v2, 32, v2
	s_waitcnt vmcnt(6)
	v_bitop3_b32 v3, v0, s22, v2 bitop3:0xde
	v_bitop3_b32 v139, s24, v0, v2 bitop3:0xf6
	s_cselect_b64 s[20:21], -1, 0
	s_add_i32 s57, 0, 0x10000
	s_add_i32 s58, 0, 0x14000
	v_or_b32_e32 v151, s23, v1
	v_add_u32_e32 v152, s57, v139
	v_add_u32_e32 v153, s58, v139
	v_add_u32_e32 v154, 0, v3
	s_movk_i32 s59, 0x300
	s_add_i32 s60, s50, 0xc000
	s_mov_b64 s[24:25], s[36:37]
	s_mov_b64 s[26:27], s[30:31]
	s_barrier
	s_branch .LBB0_778

.LBB0_1063:
	s_add_u32 s6, s18, 0x38000000
	s_addc_u32 s7, s19, 0
	s_add_u32 s8, s18, 2.0
	s_addc_u32 s9, s19, 0
	s_add_u32 s12, s18, 4.0
	s_addc_u32 s13, s19, 0
	s_and_b32 s21, s14, 3
	s_mov_b64 s[14:15], 0x80
	s_add_i32 m0, s47, 0x18000
	v_lshl_add_u64 v[6:7], v[6:7], 0, s[14:15]
	s_lshl_b32 s24, s17, 13
	s_lshl_b32 s25, s21, 12
	global_load_lds_dwordx4 v[6:7], off
	v_lshl_add_u64 v[4:5], v[4:5], 0, s[14:15]
	s_add_i32 m0, s47, 0x1a000
	s_add_i32 s53, s47, 0x8000
	s_add_i32 s54, s47, 0xa000
	global_load_lds_dwordx4 v[4:5], off
	v_lshl_add_u64 v[0:1], v[0:1], 0, s[14:15]
	s_mov_b32 m0, s53
	s_add_u32 s22, s38, 0x1880
	global_load_lds_dwordx4 v[0:1], off
	v_lshl_add_u64 v[0:1], v[2:3], 0, s[14:15]
	s_mov_b32 m0, s54
	s_addc_u32 s23, s39, 0
	global_load_lds_dwordx4 v[0:1], off
	s_add_i32 m0, s47, 0x1c000
	v_lshl_add_u64 v[0:1], s[22:23], 0, v[130:131]
	global_load_lds_dwordx4 v[0:1], off
	v_lshl_add_u64 v[0:1], s[22:23], 0, v[134:135]
	s_add_i32 m0, s47, 0x1e000
	global_load_lds_dwordx4 v[0:1], off
	s_cmp_lg_u32 s17, 1
	s_cbranch_scc1 .Lpgh_4
	s_barrier
.Lpgh_4:
	s_waitcnt vmcnt(8)
	s_barrier
	s_cmpk_lt_u32 s16, 0x100
	v_and_b32_e32 v0, 15, v8
	v_and_b32_e32 v1, 48, v8
	v_lshl_or_b32 v138, s17, 6, v0
	s_cselect_b64 s[16:17], -1, 0
	s_add_i32 s55, s42, s20
	v_lshl_or_b32 v148, s21, 6, v1
	s_mul_i32 s21, s55, 0x30000
	s_mul_hi_i32 s20, s55, 0x30000
	s_add_u32 s18, s18, s21
	v_lshlrev_b32_e32 v2, 2, v8
	s_addc_u32 s19, s19, s20
	v_lshl_or_b32 v0, v0, 6, v1
	v_and_b32_e32 v2, 32, v2
	s_waitcnt vmcnt(6)
	s_add_u32 s56, s18, 0x1a000000
	v_bitop3_b32 v3, v0, s24, v2 bitop3:0xde
	v_bitop3_b32 v139, s25, v0, v2 bitop3:0xf6
	s_addc_u32 s57, s19, 0
	s_add_i32 s60, 0, 0x10000
	s_add_i32 s61, 0, 0x14000
	v_add_u32_e32 v140, 0, v3
	v_add_u32_e32 v151, 0xa0, v138
	v_add_u32_e32 v141, 0xb0, v138
	s_mul_hi_i32 s58, s42, 0x30000
	s_mul_i32 s59, s42, 0x30000
	v_add_u32_e32 v149, s60, v139
	v_add_u32_e32 v150, s61, v139
	s_mov_b64 s[18:19], 0x100
	s_mov_b64 s[20:21], 0x180
	s_mov_b64 s[22:23], 0x200
	s_mov_b64 s[24:25], 0x280
	s_add_i32 s62, s47, 0xc000
	s_add_i32 s63, s47, 0xe000
	s_mov_b64 s[28:29], s[38:39]
	s_mov_b64 s[26:27], s[36:37]
	s_barrier
	s_branch .LBB0_1066

.LBB0_1237:
	s_add_u32 s8, s12, 0x2a000000
	s_addc_u32 s9, s13, 0
	s_add_u32 s12, s12, 0x4b200000
	s_addc_u32 s13, s13, 0
	s_lshl_b32 s14, s14, 5
	s_and_b32 s20, s14, 0x60
	s_mov_b64 s[14:15], 0x80
	s_add_i32 m0, s27, 0x18000
	v_lshl_add_u64 v[6:7], v[6:7], 0, s[14:15]
	s_lshl_b32 s17, s16, 13
	s_lshl_b32 s21, s20, 7
	global_load_lds_dwordx4 v[6:7], off
	v_lshl_add_u64 v[4:5], v[4:5], 0, s[14:15]
	s_add_i32 m0, s27, 0x1a000
	s_add_i32 s53, s27, 0x8000
	s_add_i32 s54, s27, 0xa000
	global_load_lds_dwordx4 v[4:5], off
	v_lshl_add_u64 v[0:1], v[0:1], 0, s[14:15]
	s_mov_b32 m0, s53
	s_add_u32 s18, s30, 0x40080
	global_load_lds_dwordx4 v[0:1], off
	v_lshl_add_u64 v[0:1], v[2:3], 0, s[14:15]
	s_mov_b32 m0, s54
	s_addc_u32 s19, s31, 0
	global_load_lds_dwordx4 v[0:1], off
	s_add_i32 m0, s27, 0x1c000
	v_lshl_add_u64 v[0:1], s[18:19], 0, v[132:133]
	global_load_lds_dwordx4 v[0:1], off
	v_lshl_add_u64 v[0:1], s[18:19], 0, v[128:129]
	s_add_i32 m0, s27, 0x1e000
	s_mov_b64 s[18:19], 0x40080
	global_load_lds_dwordx4 v[0:1], off
	s_cmp_lg_u32 s16, 1
	s_cbranch_scc1 .Lpgh_5
	s_barrier
.Lpgh_5:
	s_waitcnt vmcnt(8)
	s_barrier
	v_lshrrev_b32_e32 v1, 1, v9
	v_and_b32_e32 v1, 24, v1
	v_and_b32_e32 v0, 15, v9
	v_lshlrev_b32_e32 v2, 1, v1
	v_lshl_or_b32 v149, s16, 6, v0
	v_lshl_or_b32 v0, v0, 6, v2
	v_lshlrev_b32_e32 v2, 2, v9
	v_and_b32_e32 v2, 32, v2
	v_bitop3_b32 v3, v0, s17, v2 bitop3:0xde
	v_bitop3_b32 v153, s21, v0, v2 bitop3:0xf6
	v_lshlrev_b32_e32 v0, 4, v12
	v_and_b32_e32 v0, 0xffff8000, v0
	v_lshlrev_b32_e32 v2, 11, v13
	v_or3_b32 v0, v10, v0, v2
	v_or_b32_e32 v154, s20, v1
	v_add_u32_e32 v0, v0, v11
	v_mov_b32_e32 v1, v133
	v_lshl_add_u64 v[136:137], v[0:1], 0, s[18:19]
	v_lshlrev_b32_e32 v0, 4, v8
	v_and_b32_e32 v0, 0xffff8000, v0
	s_waitcnt vmcnt(6)
	s_cmpk_lt_u32 s3, 0x100
	v_or3_b32 v0, v10, v0, v2
	s_cselect_b64 s[16:17], -1, 0
	v_add_u32_e32 v0, v0, v11
	s_add_i32 s57, 0, 0x10000
	s_add_i32 s58, 0, 0x14000
	s_sext_i32_i8 s60, s2
	s_mov_b32 s55, 0
	s_ashr_i32 s56, s42, 31
	v_lshl_add_u64 v[138:139], v[0:1], 0, s[18:19]
	v_mov_b64_e32 v[140:141], 0x180
	v_mov_b64_e32 v[142:143], 0x17f
	v_add_u32_e32 v155, s57, v153
	v_add_u32_e32 v156, s58, v153
	v_add_u32_e32 v157, 0, v3
	s_movk_i32 s59, 0x600
	s_mov_b64 s[24:25], s[30:31]
	s_mov_b64 s[22:23], s[28:29]
	s_barrier
	s_branch .LBB0_1240

.LBB0_1399:
	s_add_u32 s8, s8, 0x2d000000
	s_addc_u32 s9, s9, 0
	s_and_b32 s17, s12, 3
	s_mov_b64 s[12:13], 0x80
	s_add_i32 m0, s42, 0x18000
	v_lshl_add_u64 v[6:7], v[6:7], 0, s[12:13]
	s_lshl_b32 s15, s3, 13
	s_lshl_b32 s24, s17, 12
	global_load_lds_dwordx4 v[6:7], off
	v_lshl_add_u64 v[4:5], v[4:5], 0, s[12:13]
	s_add_i32 m0, s42, 0x1a000
	s_add_i32 s48, s42, 0x8000
	s_add_i32 s49, s42, 0xa000
	global_load_lds_dwordx4 v[4:5], off
	v_lshl_add_u64 v[0:1], v[0:1], 0, s[12:13]
	s_mov_b32 m0, s48
	s_add_u32 s18, s22, 0x1880
	global_load_lds_dwordx4 v[0:1], off
	v_lshl_add_u64 v[0:1], v[2:3], 0, s[12:13]
	s_mov_b32 m0, s49
	s_addc_u32 s19, s23, 0
	global_load_lds_dwordx4 v[0:1], off
	s_add_i32 m0, s42, 0x1c000
	v_lshl_add_u64 v[0:1], s[18:19], 0, v[132:133]
	global_load_lds_dwordx4 v[0:1], off
	v_lshl_add_u64 v[0:1], s[18:19], 0, v[128:129]
	s_add_i32 m0, s42, 0x1e000
	v_lshlrev_b32_e32 v2, 2, v9
	global_load_lds_dwordx4 v[0:1], off
	s_cmp_lg_u32 s3, 1
	s_cbranch_scc1 .Lpgh_6
	s_barrier
.Lpgh_6:
	s_waitcnt vmcnt(8)
	s_barrier
	v_and_b32_e32 v0, 48, v9
	v_and_b32_e32 v1, 15, v9
	v_lshl_or_b32 v144, s3, 6, v1
	v_lshl_or_b32 v1, v1, 6, v0
	v_lshl_or_b32 v146, s17, 6, v0
	v_lshrrev_b32_e32 v0, 11, v12
	v_mul_u32_u24_e32 v0, 0x3000, v0
	v_or_b32_e32 v0, v10, v0
	v_and_b32_e32 v2, 32, v2
	v_mad_u32_u24 v0, v13, s16, v0
	v_bitop3_b32 v3, v1, s15, v2 bitop3:0xde
	v_bitop3_b32 v145, s24, v1, v2 bitop3:0xf6
	s_cmpk_lt_u32 s2, 0x100
	v_add_lshl_u32 v0, v0, v11, 1
	v_mov_b32_e32 v1, v133
	s_mov_b64 s[2:3], 0x30080
	v_lshl_add_u64 v[136:137], v[0:1], 0, s[2:3]
	v_lshrrev_b32_e32 v0, 11, v8
	v_mul_u32_u24_e32 v0, 0x3000, v0
	v_or_b32_e32 v0, v10, v0
	s_waitcnt vmcnt(6)
	v_mad_u32_u24 v0, v13, s16, v0
	s_sext_i32_i8 s58, s14
	s_cselect_b64 s[14:15], -1, 0
	v_add_lshl_u32 v0, v0, v11, 1
	s_add_i32 s52, 0, 0x10000
	s_add_i32 s53, 0, 0x14000
	s_mov_b32 s50, 0
	s_ashr_i32 s51, s29, 31
	v_lshl_add_u64 v[138:139], v[0:1], 0, s[2:3]
	v_mov_b64_e32 v[140:141], 0x300
	v_mov_b64_e32 v[142:143], 0x2ff
	v_add_u32_e32 v147, s52, v145
	v_add_u32_e32 v148, s53, v145
	v_add_u32_e32 v149, 0, v3
	s_movk_i32 s54, 0x600
	s_mov_b64 s[18:19], s[22:23]
	s_mov_b64 s[16:17], s[20:21]
	s_barrier
	s_branch .LBB0_1402

.LBB0_1419:
	s_add_u32 s8, s8, 0x33000000
	s_addc_u32 s9, s9, 0
	s_and_b32 s18, s12, 3
	s_mov_b64 s[12:13], 0x80
	s_add_i32 m0, s54, 0x18000
	v_lshl_add_u64 v[6:7], v[6:7], 0, s[12:13]
	s_lshl_b32 s15, s3, 13
	s_lshl_b32 s19, s18, 12
	global_load_lds_dwordx4 v[6:7], off
	v_lshl_add_u64 v[4:5], v[4:5], 0, s[12:13]
	s_add_i32 m0, s54, 0x1a000
	s_add_i32 s59, s54, 0x8000
	s_add_i32 s60, s54, 0xa000
	global_load_lds_dwordx4 v[4:5], off
	v_lshl_add_u64 v[0:1], v[0:1], 0, s[12:13]
	s_mov_b32 m0, s59
	s_add_u32 s16, s24, 0x1080
	global_load_lds_dwordx4 v[0:1], off
	v_lshl_add_u64 v[0:1], v[2:3], 0, s[12:13]
	s_mov_b32 m0, s60
	s_addc_u32 s17, s25, 0
	global_load_lds_dwordx4 v[0:1], off
	s_add_i32 m0, s54, 0x1c000
	v_lshl_add_u64 v[0:1], s[16:17], 0, v[130:131]
	global_load_lds_dwordx4 v[0:1], off
	v_lshl_add_u64 v[0:1], s[16:17], 0, v[134:135]
	s_add_i32 m0, s54, 0x1e000
	v_lshlrev_b32_e32 v2, 2, v8
	global_load_lds_dwordx4 v[0:1], off
	s_cmp_lg_u32 s3, 1
	s_cbranch_scc1 .Lpgh_7
	s_barrier
.Lpgh_7:
	s_waitcnt vmcnt(8)
	s_barrier
	v_and_b32_e32 v0, 48, v8
	v_and_b32_e32 v1, 15, v8
	v_lshl_or_b32 v140, s3, 6, v1
	v_lshl_or_b32 v1, v1, 6, v0
	v_and_b32_e32 v2, 32, v2
	s_waitcnt vmcnt(6)
	s_cmpk_lt_u32 s14, 0x100
	v_bitop3_b32 v3, v1, s15, v2 bitop3:0xde
	v_bitop3_b32 v141, s19, v1, v2 bitop3:0xf6
	s_cselect_b64 s[14:15], -1, 0
	s_add_i32 s62, 0, 0x10000
	s_add_i32 s63, 0, 0x14000
	s_sext_i32_i8 s69, s2
	s_ashr_i32 s61, s46, 31
	v_lshl_or_b32 v142, s18, 6, v0
	v_mov_b64_e32 v[136:137], 0x400
	v_mov_b64_e32 v[138:139], 0x3ff
	v_add_u32_e32 v143, s62, v141
	v_add_u32_e32 v144, s63, v141
	v_add_u32_e32 v145, 0, v3
	s_mov_b32 s64, 0x40000
	s_mov_b32 s65, 0x48000
	s_mov_b32 s66, 0x50000
	s_mov_b64 s[18:19], s[22:23]
	s_mov_b64 s[20:21], s[24:25]
	s_barrier
	s_branch .LBB0_1422

.LBB0_1825:
	v_bfe_u32 v82, v8, 4, 2
	v_and_b32_e32 v10, 15, v8
	v_lshlrev_b32_e32 v11, 4, v82
	v_lshlrev_b32_e32 v8, 2, v8
	s_and_b32 s55, s2, 3
	v_lshl_or_b32 v81, s3, 6, v10
	v_lshl_or_b32 v10, v10, 6, v11
	s_lshl_b32 s2, s3, 13
	v_and_b32_e32 v8, 32, v8
	v_bitop3_b32 v12, v10, s2, v8 bitop3:0xde
	s_lshl_b32 s2, s55, 12
	v_bitop3_b32 v83, v10, s2, v8 bitop3:0xde
	s_add_u32 s2, s30, 0x1e80080
	s_addc_u32 s3, s31, 0
	s_add_i32 m0, s9, 0x18000
	v_lshl_add_u64 v[10:11], s[2:3], 0, v[64:65]
	global_load_lds_dwordx4 v[10:11], off
	v_lshl_add_u64 v[10:11], s[2:3], 0, v[66:67]
	s_add_i32 m0, s9, 0x1a000
	s_mov_b64 s[16:17], 0x80
	s_add_i32 s59, s9, 0x8000
	s_add_i32 s60, s9, 0xa000
	global_load_lds_dwordx4 v[10:11], off
	v_lshl_add_u64 v[0:1], v[0:1], 0, s[16:17]
	s_mov_b32 m0, s59
	s_add_u32 s2, s30, 0x1ec0080
	global_load_lds_dwordx4 v[0:1], off
	v_lshl_add_u64 v[0:1], v[2:3], 0, s[16:17]
	s_mov_b32 m0, s60
	s_addc_u32 s3, s31, 0
	s_add_i32 s61, s9, 0x1c000
	global_load_lds_dwordx4 v[0:1], off
	v_lshl_add_u64 v[0:1], s[2:3], 0, v[64:65]
	s_mov_b32 m0, s61
	s_add_i32 s62, s9, 0x1e000
	global_load_lds_dwordx4 v[0:1], off
	v_lshl_add_u64 v[0:1], s[2:3], 0, v[66:67]
	s_mov_b32 m0, s62
	v_lshlrev_b32_e32 v2, 11, v7
	global_load_lds_dwordx4 v[0:1], off
	s_cmp_eq_u64 s[14:15], 0
	s_cbranch_scc1 .Lpgh_9
	s_barrier

.Lpgh_11:
	s_waitcnt vmcnt(8)
	s_barrier
	s_cmpk_lt_u32 s16, 0x100
	v_and_b32_e32 v0, 15, v8
	v_and_b32_e32 v1, 48, v8
	v_lshl_or_b32 v138, s17, 6, v0
	s_cselect_b64 s[16:17], -1, 0
	s_add_i32 s55, s42, s20
	v_lshl_or_b32 v148, s21, 6, v1
	s_mul_i32 s21, s55, 0x30000
	s_mul_hi_i32 s20, s55, 0x30000
	s_add_u32 s18, s18, s21
	v_lshlrev_b32_e32 v2, 2, v8
	s_addc_u32 s19, s19, s20
	v_lshl_or_b32 v0, v0, 6, v1
	v_and_b32_e32 v2, 32, v2
	s_waitcnt vmcnt(6)
	s_add_u32 s56, s18, 0x1d000000
	v_bitop3_b32 v3, v0, s24, v2 bitop3:0xde
	v_bitop3_b32 v139, s25, v0, v2 bitop3:0xf6
	s_addc_u32 s57, s19, 0
	s_add_i32 s60, 0, 0x10000
	s_add_i32 s61, 0, 0x14000
	v_add_u32_e32 v140, 0, v3
	v_add_u32_e32 v151, 0xa0, v138
	v_add_u32_e32 v141, 0xb0, v138
	s_mul_hi_i32 s58, s42, 0x30000
	s_mul_i32 s59, s42, 0x30000
	v_add_u32_e32 v149, s60, v139
	v_add_u32_e32 v150, s61, v139
	s_mov_b64 s[18:19], 0x100
	s_mov_b64 s[20:21], 0x180
	s_mov_b64 s[22:23], 0x200
	s_mov_b64 s[24:25], 0x280
	s_add_i32 s62, s47, 0xc000
	s_add_i32 s63, s47, 0xe000
	s_mov_b64 s[28:29], s[38:39]
	s_mov_b64 s[26:27], s[36:37]
	s_barrier
	s_branch .LBB0_2356

.LBB0_2809:
	v_bfe_u32 v82, v8, 4, 2
	v_and_b32_e32 v10, 15, v8
	v_lshlrev_b32_e32 v11, 4, v82
	v_lshlrev_b32_e32 v8, 2, v8
	s_and_b32 s55, s2, 3
	v_lshl_or_b32 v81, s3, 6, v10
	v_lshl_or_b32 v10, v10, 6, v11
	s_lshl_b32 s2, s3, 13
	v_and_b32_e32 v8, 32, v8
	v_bitop3_b32 v12, v10, s2, v8 bitop3:0xde
	s_lshl_b32 s2, s55, 12
	v_bitop3_b32 v83, v10, s2, v8 bitop3:0xde
	s_add_u32 s2, s30, 0x1f00080
	s_addc_u32 s3, s31, 0
	s_add_i32 m0, s9, 0x18000
	v_lshl_add_u64 v[10:11], s[2:3], 0, v[64:65]
	global_load_lds_dwordx4 v[10:11], off
	v_lshl_add_u64 v[10:11], s[2:3], 0, v[66:67]
	s_add_i32 m0, s9, 0x1a000
	s_mov_b64 s[16:17], 0x80
	s_add_i32 s59, s9, 0x8000
	s_add_i32 s60, s9, 0xa000
	global_load_lds_dwordx4 v[10:11], off
	v_lshl_add_u64 v[0:1], v[0:1], 0, s[16:17]
	s_mov_b32 m0, s59
	s_add_u32 s2, s30, 0x1f40080
	global_load_lds_dwordx4 v[0:1], off
	v_lshl_add_u64 v[0:1], v[2:3], 0, s[16:17]
	s_mov_b32 m0, s60
	s_addc_u32 s3, s31, 0
	s_add_i32 s61, s9, 0x1c000
	global_load_lds_dwordx4 v[0:1], off
	v_lshl_add_u64 v[0:1], s[2:3], 0, v[64:65]
	s_mov_b32 m0, s61
	s_add_i32 s62, s9, 0x1e000
	global_load_lds_dwordx4 v[0:1], off
	v_lshl_add_u64 v[0:1], s[2:3], 0, v[66:67]
	s_mov_b32 m0, s62
	v_lshlrev_b32_e32 v2, 11, v7
	global_load_lds_dwordx4 v[0:1], off
	s_cmp_eq_u64 s[14:15], 0
	s_cbranch_scc1 .Lpgh_14
	s_barrier

.Lpgh_16:
	s_waitcnt vmcnt(8)
	s_barrier
	s_cmpk_lt_u32 s16, 0x100
	v_and_b32_e32 v0, 15, v8
	v_and_b32_e32 v1, 48, v8
	v_lshl_or_b32 v138, s17, 6, v0
	s_cselect_b64 s[16:17], -1, 0
	s_add_i32 s55, s42, s20
	v_lshl_or_b32 v148, s21, 6, v1
	s_mul_i32 s21, s55, 0x30000
	s_mul_hi_i32 s20, s55, 0x30000
	s_add_u32 s18, s18, s21
	v_lshlrev_b32_e32 v2, 2, v8
	s_addc_u32 s19, s19, s20
	v_lshl_or_b32 v0, v0, 6, v1
	v_and_b32_e32 v2, 32, v2
	s_waitcnt vmcnt(6)
	s_add_u32 s56, s18, 0x20000000
	v_bitop3_b32 v3, v0, s24, v2 bitop3:0xde
	v_bitop3_b32 v139, s25, v0, v2 bitop3:0xf6
	s_addc_u32 s57, s19, 0
	s_add_i32 s60, 0, 0x10000
	s_add_i32 s61, 0, 0x14000
	v_add_u32_e32 v140, 0, v3
	v_add_u32_e32 v151, 0xa0, v138
	v_add_u32_e32 v141, 0xb0, v138
	s_mul_hi_i32 s58, s42, 0x30000
	s_mul_i32 s59, s42, 0x30000
	v_add_u32_e32 v149, s60, v139
	v_add_u32_e32 v150, s61, v139
	s_mov_b64 s[18:19], 0x100
	s_mov_b64 s[20:21], 0x180
	s_mov_b64 s[22:23], 0x200
	s_mov_b64 s[24:25], 0x280
	s_add_i32 s62, s47, 0xc000
	s_add_i32 s63, s47, 0xe000
	s_mov_b64 s[28:29], s[38:39]
	s_mov_b64 s[26:27], s[36:37]
	s_barrier
	s_branch .LBB0_3340

.LBB0_4099:
	v_bfe_u32 v82, v8, 4, 2
	v_and_b32_e32 v10, 15, v8
	v_lshlrev_b32_e32 v11, 4, v82
	v_lshlrev_b32_e32 v8, 2, v8
	s_and_b32 s55, s2, 3
	v_lshl_or_b32 v81, s3, 6, v10
	v_lshl_or_b32 v10, v10, 6, v11
	s_lshl_b32 s2, s3, 13
	v_and_b32_e32 v8, 32, v8
	v_bitop3_b32 v12, v10, s2, v8 bitop3:0xde
	s_lshl_b32 s2, s55, 12
	v_bitop3_b32 v83, v10, s2, v8 bitop3:0xde
	s_add_u32 s2, s30, 0x1f80080
	s_addc_u32 s3, s31, 0
	s_add_i32 m0, s9, 0x18000
	v_lshl_add_u64 v[10:11], s[2:3], 0, v[64:65]
	global_load_lds_dwordx4 v[10:11], off
	v_lshl_add_u64 v[10:11], s[2:3], 0, v[66:67]
	s_add_i32 m0, s9, 0x1a000
	s_mov_b64 s[16:17], 0x80
	s_add_i32 s59, s9, 0x8000
	s_add_i32 s60, s9, 0xa000
	global_load_lds_dwordx4 v[10:11], off
	v_lshl_add_u64 v[0:1], v[0:1], 0, s[16:17]
	s_mov_b32 m0, s59
	s_add_u32 s2, s30, 0x1fc0080
	global_load_lds_dwordx4 v[0:1], off
	v_lshl_add_u64 v[0:1], v[2:3], 0, s[16:17]
	s_mov_b32 m0, s60
	s_addc_u32 s3, s31, 0
	s_add_i32 s61, s9, 0x1c000
	global_load_lds_dwordx4 v[0:1], off
	v_lshl_add_u64 v[0:1], s[2:3], 0, v[64:65]
	s_mov_b32 m0, s61
	s_add_i32 s62, s9, 0x1e000
	global_load_lds_dwordx4 v[0:1], off
	v_lshl_add_u64 v[0:1], s[2:3], 0, v[66:67]
	s_mov_b32 m0, s62
	v_lshlrev_b32_e32 v2, 11, v7
	global_load_lds_dwordx4 v[0:1], off
	s_cmp_eq_u64 s[14:15], 0
	s_cbranch_scc1 .Lpgh_21
	s_barrier

.LBB0_4339:
	s_add_u32 s14, s2, 0x34000000
	s_addc_u32 s15, s3, 0
	s_add_u32 s16, s2, 0x41000000
	s_addc_u32 s17, s3, 0
	s_lshl_b32 s2, s18, 5
	s_mov_b64 s[18:19], 0x80
	s_and_b32 s23, s2, 0x60
	s_add_i32 m0, s49, 0x18000
	v_lshl_add_u64 v[6:7], v[6:7], 0, s[18:19]
	s_lshl_b32 s22, s21, 13
	s_lshl_b32 s24, s23, 7
	global_load_lds_dwordx4 v[6:7], off
	v_lshl_add_u64 v[4:5], v[4:5], 0, s[18:19]
	s_add_i32 m0, s49, 0x1a000
	s_add_i32 s54, s49, 0x8000
	s_add_i32 s55, s49, 0xa000
	global_load_lds_dwordx4 v[4:5], off
	v_lshl_add_u64 v[0:1], v[0:1], 0, s[18:19]
	s_mov_b32 m0, s54
	s_add_u32 s2, s36, 0x40080
	global_load_lds_dwordx4 v[0:1], off
	v_lshl_add_u64 v[0:1], v[2:3], 0, s[18:19]
	s_mov_b32 m0, s55
	s_addc_u32 s3, s37, 0
	global_load_lds_dwordx4 v[0:1], off
	s_add_i32 m0, s49, 0x1c000
	v_lshl_add_u64 v[0:1], s[2:3], 0, v[128:129]
	global_load_lds_dwordx4 v[0:1], off
	v_lshl_add_u64 v[0:1], s[2:3], 0, v[130:131]
	s_add_i32 m0, s49, 0x1e000
	global_load_lds_dwordx4 v[0:1], off
	s_cmp_lg_u32 s21, 1
	s_cbranch_scc1 .Lpgh_22
	s_barrier
.Lpgh_22:
	s_waitcnt vmcnt(8)
	s_barrier
	s_cmpk_lt_u32 s20, 0x100
	v_lshrrev_b32_e32 v1, 1, v8
	v_and_b32_e32 v1, 24, v1
	v_and_b32_e32 v0, 15, v8
	v_lshlrev_b32_e32 v2, 1, v1
	v_lshl_or_b32 v137, s21, 6, v0
	v_lshl_or_b32 v0, v0, 6, v2
	v_lshlrev_b32_e32 v2, 2, v8
	v_and_b32_e32 v2, 32, v2
	s_waitcnt vmcnt(6)
	v_bitop3_b32 v3, v0, s22, v2 bitop3:0xde
	v_bitop3_b32 v139, s24, v0, v2 bitop3:0xf6
	s_cselect_b64 s[20:21], -1, 0
	s_add_i32 s56, 0, 0x10000
	s_add_i32 s57, 0, 0x14000
	v_or_b32_e32 v151, s23, v1
	v_add_u32_e32 v152, s56, v139
	v_add_u32_e32 v153, s57, v139
	v_add_u32_e32 v154, 0, v3
	s_movk_i32 s58, 0x300
	s_add_i32 s59, s49, 0xc000
	s_mov_b64 s[24:25], s[36:37]
	s_mov_b64 s[26:27], s[30:31]
	s_barrier
	s_branch .LBB0_4342

.LBB0_4454:
	s_add_u32 s6, s18, 0x38000000
	s_addc_u32 s7, s19, 0
	s_add_u32 s8, s18, 2.0
	s_addc_u32 s9, s19, 0
	s_add_u32 s12, s18, 4.0
	s_addc_u32 s13, s19, 0
	s_and_b32 s21, s14, 3
	s_mov_b64 s[14:15], 0x80
	s_add_i32 m0, s46, 0x18000
	v_lshl_add_u64 v[6:7], v[6:7], 0, s[14:15]
	s_lshl_b32 s24, s17, 13
	s_lshl_b32 s25, s21, 12
	global_load_lds_dwordx4 v[6:7], off
	v_lshl_add_u64 v[4:5], v[4:5], 0, s[14:15]
	s_add_i32 m0, s46, 0x1a000
	s_add_i32 s52, s46, 0x8000
	s_add_i32 s53, s46, 0xa000
	global_load_lds_dwordx4 v[4:5], off
	v_lshl_add_u64 v[0:1], v[0:1], 0, s[14:15]
	s_mov_b32 m0, s52
	s_add_u32 s22, s38, 0x1880
	global_load_lds_dwordx4 v[0:1], off
	v_lshl_add_u64 v[0:1], v[2:3], 0, s[14:15]
	s_mov_b32 m0, s53
	s_addc_u32 s23, s39, 0
	global_load_lds_dwordx4 v[0:1], off
	s_add_i32 m0, s46, 0x1c000
	v_lshl_add_u64 v[0:1], s[22:23], 0, v[130:131]
	global_load_lds_dwordx4 v[0:1], off
	v_lshl_add_u64 v[0:1], s[22:23], 0, v[134:135]
	s_add_i32 m0, s46, 0x1e000
	global_load_lds_dwordx4 v[0:1], off
	s_cmp_lg_u32 s17, 1
	s_cbranch_scc1 .Lpgh_23
	s_barrier
.Lpgh_23:
	s_waitcnt vmcnt(8)
	s_barrier
	s_cmpk_lt_u32 s16, 0x100
	v_and_b32_e32 v0, 15, v8
	v_and_b32_e32 v1, 48, v8
	v_lshl_or_b32 v138, s17, 6, v0
	s_cselect_b64 s[16:17], -1, 0
	s_add_i32 s54, s41, s20
	v_lshl_or_b32 v148, s21, 6, v1
	s_mul_i32 s21, s54, 0x30000
	s_mul_hi_i32 s20, s54, 0x30000
	s_add_u32 s18, s18, s21
	v_lshlrev_b32_e32 v2, 2, v8
	s_addc_u32 s19, s19, s20
	v_lshl_or_b32 v0, v0, 6, v1
	v_and_b32_e32 v2, 32, v2
	s_waitcnt vmcnt(6)
	s_add_u32 s55, s18, 0x23000000
	v_bitop3_b32 v3, v0, s24, v2 bitop3:0xde
	v_bitop3_b32 v139, s25, v0, v2 bitop3:0xf6
	s_addc_u32 s56, s19, 0
	s_add_i32 s59, 0, 0x10000
	s_add_i32 s60, 0, 0x14000
	v_add_u32_e32 v140, 0, v3
	v_add_u32_e32 v151, 0xa0, v138
	v_add_u32_e32 v141, 0xb0, v138
	s_mul_hi_i32 s57, s41, 0x30000
	s_mul_i32 s58, s41, 0x30000
	v_add_u32_e32 v149, s59, v139
	v_add_u32_e32 v150, s60, v139
	s_mov_b64 s[18:19], 0x100
	s_mov_b64 s[20:21], 0x180
	s_mov_b64 s[22:23], 0x200
	s_mov_b64 s[24:25], 0x280
	s_add_i32 s61, s46, 0xc000
	s_add_i32 s62, s46, 0xe000
	s_mov_b64 s[28:29], s[38:39]
	s_mov_b64 s[26:27], s[36:37]
	s_barrier
	s_branch .LBB0_4457
